# v82 + T-phase gate reuse: denominators of epilogue z kept in free VGPRs as numerators of z+1; z>=1 epilogue copy issues all remaining gate loads up front
# baseline (speedup 1.0000x reference)
.LBB0_868:
	s_cmp_eq_u32 s38, 0
	s_cbranch_scc0 .Ltb_entry
	s_lshl_b32 s2, s38, 2
	s_ashr_i32 s3, s2, 31
	s_lshl_b64 s[92:93], s[2:3], 16
	s_cmp_lt_i32 s38, 3
	s_cselect_b64 s[22:23], -1, 0
	s_cmp_gt_i32 s38, 2
	s_cselect_b64 s[2:3], -1, 0
	s_add_u32 s90, s92, 0x40000
	s_addc_u32 s91, s93, 0
	s_lshl_b32 s39, s95, 4
	s_add_i32 s42, s39, s87
	s_ashr_i32 s43, s42, 31
	s_lshl_b64 s[42:43], s[42:43], 16
	v_lshl_add_u64 v[148:149], v[132:133], 0, s[42:43]
	v_mov_b64_e32 v[138:139], v[148:149]
	s_and_b64 vcc, exec, s[2:3]
	v_lshl_add_u64 v[136:137], v[138:139], 0, s[92:93]
	global_load_dwordx2 v[156:157], v[136:137], off
	v_lshl_add_u64 v[140:141], v[138:139], 0, s[90:91]
	s_cbranch_vccnz .LBB0_870
	global_load_dwordx2 v[146:147], v[140:141], off

.LBB0_874:
	s_waitcnt vmcnt(0)
	v_mov_b32_e32 v212, v146
	v_mov_b32_e32 v213, v147
	v_mov_b32_e32 v214, v144
	v_mov_b32_e32 v215, v145
	v_mov_b32_e32 v216, v138
	v_mov_b32_e32 v217, v139
	v_mov_b32_e32 v218, v136
	v_mov_b32_e32 v219, v137
	v_cvt_f32_ubyte1_e32 v141, v156
	v_cvt_f32_ubyte0_e32 v140, v156
	v_cvt_f32_ubyte3_e32 v143, v156
	v_cvt_f32_ubyte2_e32 v142, v156
	v_cndmask_b32_e64 v156, 0, 1, s[2:3]
	v_cvt_f32_ubyte1_e32 v163, v157
	v_cvt_f32_ubyte0_e32 v162, v157
	v_cvt_f32_ubyte3_e32 v167, v157
	v_cvt_f32_ubyte2_e32 v166, v157
	v_cmp_ne_u32_e64 s[42:43], 1, v156
	s_andn2_b64 vcc, exec, s[2:3]
	s_mov_b64 s[2:3], -1
	s_cbranch_vccnz .LBB0_876
	v_pk_mul_f32 v[156:157], v[166:167], s[82:83] op_sel_hi:[1,0]
	v_pk_mul_f32 v[158:159], v[162:163], s[82:83] op_sel_hi:[1,0]
	v_pk_mul_f32 v[164:165], v[142:143], s[82:83] op_sel_hi:[1,0]
	v_pk_mul_f32 v[168:169], v[140:141], s[82:83] op_sel_hi:[1,0]
	s_mov_b64 s[2:3], 0

.LBB0_908:
	s_waitcnt vmcnt(0)
	v_mov_b32_e32 v220, v146
	v_mov_b32_e32 v221, v147
	v_mov_b32_e32 v222, v144
	v_mov_b32_e32 v223, v145
	v_mov_b32_e32 v224, v138
	v_mov_b32_e32 v228, v139
	v_mov_b32_e32 v229, v136
	v_mov_b32_e32 v231, v137
	v_cvt_f32_ubyte1_e32 v157, v158
	v_cvt_f32_ubyte0_e32 v156, v158
	v_cvt_f32_ubyte3_e32 v163, v158
	v_cvt_f32_ubyte2_e32 v162, v158
	v_cvt_f32_ubyte1_e32 v165, v159
	v_cvt_f32_ubyte0_e32 v164, v159
	v_cvt_f32_ubyte3_e32 v169, v159
	v_cvt_f32_ubyte2_e32 v168, v159
	s_and_b64 vcc, exec, s[42:43]
	s_mov_b64 s[2:3], -1
	s_cbranch_vccnz .LBB0_910
	v_pk_mul_f32 v[158:159], v[168:169], s[82:83] op_sel_hi:[1,0]
	v_pk_mul_f32 v[166:167], v[164:165], s[82:83] op_sel_hi:[1,0]
	v_pk_mul_f32 v[170:171], v[162:163], s[82:83] op_sel_hi:[1,0]
	v_pk_mul_f32 v[172:173], v[156:157], s[82:83] op_sel_hi:[1,0]
	s_mov_b64 s[2:3], 0

.LBB0_940:
	s_waitcnt vmcnt(0)
	v_mov_b32_e32 v232, v146
	v_mov_b32_e32 v233, v147
	v_mov_b32_e32 v234, v144
	v_mov_b32_e32 v235, v145
	v_mov_b32_e32 v236, v138
	v_mov_b32_e32 v237, v139
	v_mov_b32_e32 v238, v136
	v_mov_b32_e32 v239, v137
	v_cvt_f32_ubyte1_e32 v157, v158
	v_cvt_f32_ubyte0_e32 v156, v158
	v_cvt_f32_ubyte3_e32 v163, v158
	v_cvt_f32_ubyte2_e32 v162, v158
	v_cvt_f32_ubyte1_e32 v165, v159
	v_cvt_f32_ubyte0_e32 v164, v159
	v_cvt_f32_ubyte3_e32 v167, v159
	v_cvt_f32_ubyte2_e32 v166, v159
	s_and_b64 vcc, exec, s[42:43]
	s_mov_b64 s[2:3], -1
	s_cbranch_vccnz .LBB0_942
	v_pk_mul_f32 v[158:159], v[166:167], s[82:83] op_sel_hi:[1,0]
	v_pk_mul_f32 v[168:169], v[164:165], s[82:83] op_sel_hi:[1,0]
	v_pk_mul_f32 v[170:171], v[162:163], s[82:83] op_sel_hi:[1,0]
	v_pk_mul_f32 v[172:173], v[156:157], s[82:83] op_sel_hi:[1,0]
	s_mov_b64 s[2:3], 0

.Ltb_entry:
	s_lshl_b32 s2, s38, 2
	s_ashr_i32 s3, s2, 31
	s_lshl_b64 s[92:93], s[2:3], 16
	s_cmp_lt_i32 s38, 3
	s_cselect_b64 s[22:23], -1, 0
	s_cmp_gt_i32 s38, 2
	s_cselect_b64 s[2:3], -1, 0
	s_add_u32 s90, s92, 0x40000
	s_addc_u32 s91, s93, 0
	s_lshl_b32 s39, s95, 4
	s_add_i32 s42, s39, s87
	s_ashr_i32 s43, s42, 31
	s_lshl_b64 s[42:43], s[42:43], 16
	v_lshl_add_u64 v[148:149], v[132:133], 0, s[42:43]
	v_mov_b64_e32 v[138:139], v[148:149]
	s_and_b64 vcc, exec, s[2:3]
	v_lshl_add_u64 v[136:137], v[138:139], 0, s[92:93]
	v_mov_b32_e32 v156, v212
	v_mov_b32_e32 v157, v213
	v_lshl_add_u64 v[140:141], v[138:139], 0, s[90:91]
	s_cmp_lt_i32 s38, 3
	s_cbranch_scc0 .Ltb_nohoist
	s_mov_b64 s[98:99], 0x1000
	v_lshl_add_u64 v[142:143], v[140:141], 0, s[98:99]
	global_load_dwordx2 v[182:183], v[140:141], off
	global_load_dwordx2 v[184:185], v[140:141], off offset:512
	global_load_dwordx2 v[186:187], v[140:141], off offset:1024
	global_load_dwordx2 v[188:189], v[140:141], off offset:1536
	global_load_dwordx2 v[190:191], v[140:141], off offset:2048
	global_load_dwordx2 v[192:193], v[140:141], off offset:2560
	global_load_dwordx2 v[194:195], v[140:141], off offset:3072
	global_load_dwordx2 v[196:197], v[140:141], off offset:3584
	global_load_dwordx2 v[198:199], v[142:143], off
	global_load_dwordx2 v[200:201], v[142:143], off offset:512
	global_load_dwordx2 v[202:203], v[142:143], off offset:1024
	global_load_dwordx2 v[204:205], v[142:143], off offset:1536
	global_load_dwordx2 v[206:207], v[142:143], off offset:2048
	global_load_dwordx2 v[208:209], v[142:143], off offset:2560
	global_load_dwordx2 v[210:211], v[142:143], off offset:3072
.Ltb_nohoist:
	s_cbranch_vccnz .Ltb_870
.Ltb_870:
	v_mov_b32_e32 v154, v214
	v_mov_b32_e32 v155, v215
	v_cndmask_b32_e64 v138, 0, 1, s[22:23]
	v_cmp_ne_u32_e64 s[46:47], 1, v138
	s_andn2_b64 vcc, exec, s[22:23]
	s_cbranch_vccnz .Ltb_902
	v_mov_b32_e32 v152, v216
	v_mov_b32_e32 v153, v217
	s_and_b64 vcc, exec, s[46:47]
	s_cbranch_vccz .Ltb_903
.Ltb_872:
	v_mov_b32_e32 v150, v218
	v_mov_b32_e32 v151, v219
	s_and_b64 vcc, exec, s[46:47]
	s_cbranch_vccnz .Ltb_874
.Ltb_873:
.Ltb_874:
	s_waitcnt vmcnt(0)
	v_mov_b32_e32 v146, v182
	v_mov_b32_e32 v147, v183
	v_mov_b32_e32 v212, v182
	v_mov_b32_e32 v213, v183
	v_mov_b32_e32 v144, v184
	v_mov_b32_e32 v145, v185
	v_mov_b32_e32 v214, v184
	v_mov_b32_e32 v215, v185
	v_mov_b32_e32 v138, v186
	v_mov_b32_e32 v139, v187
	v_mov_b32_e32 v216, v186
	v_mov_b32_e32 v217, v187
	v_mov_b32_e32 v136, v188
	v_mov_b32_e32 v137, v189
	v_mov_b32_e32 v218, v188
	v_mov_b32_e32 v219, v189
	v_cvt_f32_ubyte1_e32 v141, v156
	v_cvt_f32_ubyte0_e32 v140, v156
	v_cvt_f32_ubyte3_e32 v143, v156
	v_cvt_f32_ubyte2_e32 v142, v156
	v_cndmask_b32_e64 v156, 0, 1, s[2:3]
	v_cvt_f32_ubyte1_e32 v163, v157
	v_cvt_f32_ubyte0_e32 v162, v157
	v_cvt_f32_ubyte3_e32 v167, v157
	v_cvt_f32_ubyte2_e32 v166, v157
	v_cmp_ne_u32_e64 s[42:43], 1, v156
	s_andn2_b64 vcc, exec, s[2:3]
	s_mov_b64 s[2:3], -1
	s_cbranch_vccnz .Ltb_876
	v_pk_mul_f32 v[156:157], v[166:167], s[82:83] op_sel_hi:[1,0]
	v_pk_mul_f32 v[158:159], v[162:163], s[82:83] op_sel_hi:[1,0]
	v_pk_mul_f32 v[164:165], v[142:143], s[82:83] op_sel_hi:[1,0]
	v_pk_mul_f32 v[168:169], v[140:141], s[82:83] op_sel_hi:[1,0]
	s_mov_b64 s[2:3], 0

.Ltb_898:
	v_mov_b64_e32 v[152:153], v[148:149]
	s_and_b64 vcc, exec, s[46:47]
	v_lshl_add_u64 v[150:151], v[152:153], 0, s[92:93]
	v_mov_b32_e32 v158, v220
	v_mov_b32_e32 v159, v221
	v_lshl_add_u64 v[156:157], v[152:153], 0, s[90:91]
	s_cbranch_vccnz .Ltb_904
	v_mov_b32_e32 v154, v222
	v_mov_b32_e32 v155, v223
	s_and_b64 vcc, exec, s[46:47]
	s_cbranch_vccz .Ltb_905
.Ltb_900:
	v_mov_b32_e32 v152, v224
	v_mov_b32_e32 v153, v228
	s_and_b64 vcc, exec, s[46:47]
	s_cbranch_vccnz .Ltb_906
.Ltb_901:
	s_nop 0
	v_mov_b32_e32 v150, v229
	v_mov_b32_e32 v151, v231
	s_and_b64 vcc, exec, s[46:47]
	s_cbranch_vccz .Ltb_907
	s_branch .Ltb_908
.Ltb_902:
	v_mov_b32_e32 v152, v216
	v_mov_b32_e32 v153, v217
	s_and_b64 vcc, exec, s[46:47]
	s_cbranch_vccnz .Ltb_872
.Ltb_903:
	v_mov_b32_e32 v150, v218
	v_mov_b32_e32 v151, v219
	s_and_b64 vcc, exec, s[46:47]
	s_cbranch_vccz .Ltb_873
	s_branch .Ltb_874
.Ltb_904:
	v_mov_b32_e32 v154, v222
	v_mov_b32_e32 v155, v223
	s_and_b64 vcc, exec, s[46:47]
	s_cbranch_vccnz .Ltb_900
.Ltb_905:
	v_mov_b32_e32 v152, v224
	v_mov_b32_e32 v153, v228
	s_and_b64 vcc, exec, s[46:47]
	s_cbranch_vccz .Ltb_901
.Ltb_906:
	v_mov_b32_e32 v150, v229
	v_mov_b32_e32 v151, v231
	s_and_b64 vcc, exec, s[46:47]
	s_cbranch_vccnz .Ltb_908
.Ltb_907:
.Ltb_908:
	s_waitcnt vmcnt(0)
	v_mov_b32_e32 v146, v190
	v_mov_b32_e32 v147, v191
	v_mov_b32_e32 v220, v190
	v_mov_b32_e32 v221, v191
	v_mov_b32_e32 v144, v192
	v_mov_b32_e32 v145, v193
	v_mov_b32_e32 v222, v192
	v_mov_b32_e32 v223, v193
	v_mov_b32_e32 v138, v194
	v_mov_b32_e32 v139, v195
	v_mov_b32_e32 v224, v194
	v_mov_b32_e32 v228, v195
	v_mov_b32_e32 v136, v196
	v_mov_b32_e32 v137, v197
	v_mov_b32_e32 v229, v196
	v_mov_b32_e32 v231, v197
	v_cvt_f32_ubyte1_e32 v157, v158
	v_cvt_f32_ubyte0_e32 v156, v158
	v_cvt_f32_ubyte3_e32 v163, v158
	v_cvt_f32_ubyte2_e32 v162, v158
	v_cvt_f32_ubyte1_e32 v165, v159
	v_cvt_f32_ubyte0_e32 v164, v159
	v_cvt_f32_ubyte3_e32 v169, v159
	v_cvt_f32_ubyte2_e32 v168, v159
	s_and_b64 vcc, exec, s[42:43]
	s_mov_b64 s[2:3], -1
	s_cbranch_vccnz .Ltb_910
	v_pk_mul_f32 v[158:159], v[168:169], s[82:83] op_sel_hi:[1,0]
	v_pk_mul_f32 v[166:167], v[164:165], s[82:83] op_sel_hi:[1,0]
	v_pk_mul_f32 v[170:171], v[162:163], s[82:83] op_sel_hi:[1,0]
	v_pk_mul_f32 v[172:173], v[156:157], s[82:83] op_sel_hi:[1,0]
	s_mov_b64 s[2:3], 0

.Ltb_932:
	v_mov_b64_e32 v[150:151], v[148:149]
	s_mov_b64 s[2:3], 0x1000
	s_and_b64 vcc, exec, s[46:47]
	v_lshl_add_u64 v[152:153], v[150:151], 0, s[2:3]
	v_lshl_add_u64 v[154:155], v[152:153], 0, s[92:93]
	v_mov_b32_e32 v158, v232
	v_mov_b32_e32 v159, v233
	s_cbranch_vccnz .Ltb_934
	v_lshl_add_u64 v[146:147], v[152:153], 0, s[90:91]
.Ltb_934:
	s_mov_b64 s[2:3], 0x1200
	v_lshl_add_u64 v[152:153], v[150:151], 0, s[2:3]
	v_lshl_add_u64 v[154:155], v[152:153], 0, s[92:93]
	v_mov_b32_e32 v154, v234
	v_mov_b32_e32 v155, v235
	s_and_b64 vcc, exec, s[46:47]
	s_cbranch_vccnz .Ltb_936
	v_lshl_add_u64 v[144:145], v[152:153], 0, s[90:91]
.Ltb_936:
	s_mov_b64 s[2:3], 0x1400
	v_lshl_add_u64 v[156:157], v[150:151], 0, s[2:3]
	v_lshl_add_u64 v[152:153], v[156:157], 0, s[92:93]
	v_mov_b32_e32 v152, v236
	v_mov_b32_e32 v153, v237
	s_and_b64 vcc, exec, s[46:47]
	s_cbranch_vccnz .Ltb_938
	v_lshl_add_u64 v[138:139], v[156:157], 0, s[90:91]
.Ltb_938:
	s_mov_b64 s[2:3], 0x1600
	v_lshl_add_u64 v[156:157], v[150:151], 0, s[2:3]
	v_lshl_add_u64 v[150:151], v[156:157], 0, s[92:93]
	v_mov_b32_e32 v150, v238
	v_mov_b32_e32 v151, v239
	s_and_b64 vcc, exec, s[46:47]
	s_cbranch_vccnz .Ltb_940
	v_lshl_add_u64 v[136:137], v[156:157], 0, s[90:91]
.Ltb_940:
	s_waitcnt vmcnt(0)
	v_mov_b32_e32 v146, v198
	v_mov_b32_e32 v147, v199
	v_mov_b32_e32 v232, v198
	v_mov_b32_e32 v233, v199
	v_mov_b32_e32 v144, v200
	v_mov_b32_e32 v145, v201
	v_mov_b32_e32 v234, v200
	v_mov_b32_e32 v235, v201
	v_mov_b32_e32 v138, v202
	v_mov_b32_e32 v139, v203
	v_mov_b32_e32 v236, v202
	v_mov_b32_e32 v237, v203
	v_mov_b32_e32 v136, v204
	v_mov_b32_e32 v137, v205
	v_mov_b32_e32 v238, v204
	v_mov_b32_e32 v239, v205
	v_cvt_f32_ubyte1_e32 v157, v158
	v_cvt_f32_ubyte0_e32 v156, v158
	v_cvt_f32_ubyte3_e32 v163, v158
	v_cvt_f32_ubyte2_e32 v162, v158
	v_cvt_f32_ubyte1_e32 v165, v159
	v_cvt_f32_ubyte0_e32 v164, v159
	v_cvt_f32_ubyte3_e32 v167, v159
	v_cvt_f32_ubyte2_e32 v166, v159
	s_and_b64 vcc, exec, s[42:43]
	s_mov_b64 s[2:3], -1
	s_cbranch_vccnz .Ltb_942
	v_pk_mul_f32 v[158:159], v[166:167], s[82:83] op_sel_hi:[1,0]
	v_pk_mul_f32 v[168:169], v[164:165], s[82:83] op_sel_hi:[1,0]
	v_pk_mul_f32 v[170:171], v[162:163], s[82:83] op_sel_hi:[1,0]
	v_pk_mul_f32 v[172:173], v[156:157], s[82:83] op_sel_hi:[1,0]
	s_mov_b64 s[2:3], 0

.Ltb_964:
	s_mov_b64 s[2:3], 0x1800
	s_and_b64 vcc, exec, s[46:47]
	v_lshl_add_u64 v[150:151], v[148:149], 0, s[2:3]
	v_lshl_add_u64 v[152:153], v[150:151], 0, s[92:93]
	global_load_dwordx2 v[156:157], v[152:153], off
	s_cbranch_vccnz .Ltb_966
	v_lshl_add_u64 v[146:147], v[150:151], 0, s[90:91]
.Ltb_966:
	s_mov_b64 s[2:3], 0x1a00
	v_lshl_add_u64 v[150:151], v[148:149], 0, s[2:3]
	v_lshl_add_u64 v[152:153], v[150:151], 0, s[92:93]
	global_load_dwordx2 v[152:153], v[152:153], off
	s_and_b64 vcc, exec, s[46:47]
	s_cbranch_vccnz .Ltb_968
	v_lshl_add_u64 v[144:145], v[150:151], 0, s[90:91]
.Ltb_968:
	s_mov_b64 s[2:3], 0x1c00
	v_lshl_add_u64 v[154:155], v[148:149], 0, s[2:3]
	v_lshl_add_u64 v[150:151], v[154:155], 0, s[92:93]
	global_load_dwordx2 v[150:151], v[150:151], off
	s_and_b64 vcc, exec, s[46:47]
	s_cbranch_vccnz .Ltb_970
	v_lshl_add_u64 v[138:139], v[154:155], 0, s[90:91]
.Ltb_970:
	s_mov_b64 s[2:3], 0x1e00
	v_lshl_add_u64 v[154:155], v[148:149], 0, s[2:3]
	v_lshl_add_u64 v[148:149], v[154:155], 0, s[92:93]
	global_load_dwordx2 v[148:149], v[148:149], off
	s_and_b64 vcc, exec, s[46:47]
	s_cbranch_vccnz .Ltb_972
	v_lshl_add_u64 v[136:137], v[154:155], 0, s[90:91]
	global_load_dwordx2 v[136:137], v[136:137], off
.Ltb_972:
	s_waitcnt vmcnt(0)
	v_mov_b32_e32 v146, v206
	v_mov_b32_e32 v147, v207
	v_mov_b32_e32 v144, v208
	v_mov_b32_e32 v145, v209
	v_mov_b32_e32 v138, v210
	v_mov_b32_e32 v139, v211
	v_cvt_f32_ubyte1_e32 v155, v156
	v_cvt_f32_ubyte0_e32 v154, v156
	v_cvt_f32_ubyte3_e32 v159, v156
	v_cvt_f32_ubyte2_e32 v158, v156
	v_cvt_f32_ubyte1_e32 v163, v157
	v_cvt_f32_ubyte0_e32 v162, v157
	v_cvt_f32_ubyte3_e32 v167, v157
	v_cvt_f32_ubyte2_e32 v166, v157
	s_and_b64 vcc, exec, s[42:43]
	s_mov_b64 s[2:3], -1
	s_cbranch_vccnz .Ltb_974
	v_pk_mul_f32 v[156:157], v[166:167], s[82:83] op_sel_hi:[1,0]
	v_pk_mul_f32 v[164:165], v[162:163], s[82:83] op_sel_hi:[1,0]
	v_pk_mul_f32 v[168:169], v[158:159], s[82:83] op_sel_hi:[1,0]
	v_pk_mul_f32 v[170:171], v[154:155], s[82:83] op_sel_hi:[1,0]
	s_mov_b64 s[2:3], 0

.Ltb_994:
	v_pk_mul_f32 v[120:121], v[120:121], v[154:155]
	v_pk_mul_f32 v[122:123], v[122:123], v[152:153]
	v_pk_mul_f32 v[124:125], v[124:125], v[148:149]
	s_and_b64 vcc, exec, s[44:45]
	v_pk_mul_f32 v[126:127], v[126:127], v[144:145]
	s_cbranch_vccnz .LBB0_996
	v_cvt_pk_bf16_f32 v140, v120, v121
	v_cvt_pk_bf16_f32 v141, v122, v123
	v_cvt_pk_bf16_f32 v142, v124, v125
	v_cvt_pk_bf16_f32 v143, v126, v127
	global_store_dwordx4 v[138:139], v[140:143], off offset:256
	s_branch .LBB0_996
